# speedup vs baseline: 1.0093x; 1.0093x over previous
.LBB2_48:
	v_readlane_b32 s2, v35, 0
	v_readlane_b32 s3, v35, 16
	s_max_i32 s2, s2, s3
	v_readlane_b32 s3, v35, 32
	v_readlane_b32 s4, v35, 48
	s_nop 0
	v_mov_b32_e32 v2, s3
	v_mov_b32_e32 v3, s4
	v_max3_i32 v2, s2, v2, v3
	s_mov_b32 s2, 3
	v_readfirstlane_b32 s3, v2
	s_add_i32 s3, s3, 3
	s_mul_hi_i32 s3, s3, 0x55555556
	s_lshr_b32 s4, s3, 31
	s_add_i32 s3, s3, s4
	s_mul_i32 s3, s3, 3
	s_setprio 3
	ds_read_b96 v[62:64], v70 offset:768
	s_mov_b32 s21, s44
	s_cmp_gt_i32 s3, 3
	s_cselect_b32 s4, 12, 0
	v_add_u32_e32 v73, s4, v70
	ds_read2_b32 v[78:79], v73 offset0:192 offset1:193
	ds_read_b32 v80, v73 offset:776
	v_mov_b32_e32 v22, 0
	v_mov_b32_e32 v23, v22
	v_mov_b32_e32 v24, v22
	v_mov_b32_e32 v25, v22
	v_mov_b32_e32 v26, v22
	v_mov_b32_e32 v27, v22
	v_mov_b32_e32 v28, v22
	v_mov_b32_e32 v29, v22
	v_mov_b32_e32 v30, v22
	v_mov_b32_e32 v31, v22
	v_mov_b32_e32 v32, v22
	v_mov_b32_e32 v33, v22
	v_mov_b32_e32 v34, v22
	v_mov_b32_e32 v35, v22
	v_mov_b32_e32 v36, v22
	v_mov_b32_e32 v37, v22
	v_mov_b32_e32 v38, v22
	v_mov_b32_e32 v39, v22
	v_mov_b32_e32 v40, v22
	v_mov_b32_e32 v41, v22
	v_mov_b32_e32 v42, v22
	v_mov_b32_e32 v43, v22
	v_mov_b32_e32 v44, v22
	v_mov_b32_e32 v45, v22
	v_mov_b32_e32 v46, v22
	v_mov_b32_e32 v47, v22
	v_mov_b32_e32 v48, v22
	v_mov_b32_e32 v49, v22
	v_mov_b32_e32 v50, v22
	v_mov_b32_e32 v51, v22
	v_mov_b32_e32 v52, v22
	v_mov_b32_e32 v53, v22
	v_and_b32_e32 v72, 3, v68
	v_lshl_add_u32 v72, v72, 2, v70
	s_mov_b32 s2, 0
	s_waitcnt lgkmcnt(2)
	v_lshl_or_b32 v2, v62, 8, v71
	v_lshl_or_b32 v6, v63, 8, v71
	v_lshl_or_b32 v10, v64, 8, v71
	buffer_load_dwordx4 v[2:5], v2, s[20:23], 0 offen
	buffer_load_dwordx4 v[6:9], v6, s[20:23], 0 offen
	buffer_load_dwordx4 v[10:13], v10, s[20:23], 0 offen
	s_waitcnt lgkmcnt(0)
	v_lshl_or_b32 v14, v78, 8, v71
	v_lshl_or_b32 v18, v79, 8, v71
	v_lshl_or_b32 v74, v80, 8, v71
	buffer_load_dwordx4 v[14:17], v14, s[20:23], 0 offen
	buffer_load_dwordx4 v[18:21], v18, s[20:23], 0 offen
	buffer_load_dwordx4 v[74:77], v74, s[20:23], 0 offen
.Ll1g_loopE:
	s_add_i32 s5, s2, 6
	s_cmp_ge_i32 s5, s3
	s_cbranch_scc1 .Ll1g_tailE
	ds_read_b32 v65, v72
	ds_read_b32 v66, v72 offset:16
	ds_read_b32 v67, v72 offset:32
	s_lshl_b32 s4, s5, 2
	v_add_u32_e32 v73, s4, v70
	ds_read2_b32 v[62:63], v73 offset0:192 offset1:193
	ds_read_b32 v64, v73 offset:776
	s_waitcnt vmcnt(3)
	v_cvt_f32_f16_sdwa v55, v2 dst_sel:DWORD dst_unused:UNUSED_PAD src0_sel:WORD_1
	v_cvt_f32_f16_e32 v54, v2
	v_cvt_f32_f16_sdwa v57, v3 dst_sel:DWORD dst_unused:UNUSED_PAD src0_sel:WORD_1
	v_cvt_f32_f16_e32 v56, v3
	v_cvt_f32_f16_sdwa v59, v4 dst_sel:DWORD dst_unused:UNUSED_PAD src0_sel:WORD_1
	v_cvt_f32_f16_e32 v58, v4
	v_cvt_f32_f16_sdwa v61, v5 dst_sel:DWORD dst_unused:UNUSED_PAD src0_sel:WORD_1
	v_cvt_f32_f16_e32 v60, v5
	v_cvt_f32_f16_sdwa v79, v6 dst_sel:DWORD dst_unused:UNUSED_PAD src0_sel:WORD_1
	v_cvt_f32_f16_e32 v78, v6
	v_cvt_f32_f16_sdwa v81, v7 dst_sel:DWORD dst_unused:UNUSED_PAD src0_sel:WORD_1
	v_cvt_f32_f16_e32 v80, v7
	v_cvt_f32_f16_sdwa v83, v8 dst_sel:DWORD dst_unused:UNUSED_PAD src0_sel:WORD_1
	v_cvt_f32_f16_e32 v82, v8
	v_cvt_f32_f16_sdwa v85, v9 dst_sel:DWORD dst_unused:UNUSED_PAD src0_sel:WORD_1
	v_cvt_f32_f16_e32 v84, v9
	s_waitcnt lgkmcnt(2)
	v_mfma_f32_4x4x1_16b_f32 v[22:25], v65, v54, v[22:25]
	v_mfma_f32_4x4x1_16b_f32 v[26:29], v65, v55, v[26:29]
	v_mfma_f32_4x4x1_16b_f32 v[30:33], v65, v56, v[30:33]
	v_mfma_f32_4x4x1_16b_f32 v[34:37], v65, v57, v[34:37]
	v_mfma_f32_4x4x1_16b_f32 v[38:41], v65, v58, v[38:41]
	v_mfma_f32_4x4x1_16b_f32 v[42:45], v65, v59, v[42:45]
	v_mfma_f32_4x4x1_16b_f32 v[46:49], v65, v60, v[46:49]
	v_mfma_f32_4x4x1_16b_f32 v[50:53], v65, v61, v[50:53]
	v_cvt_f32_f16_sdwa v87, v10 dst_sel:DWORD dst_unused:UNUSED_PAD src0_sel:WORD_1
	v_cvt_f32_f16_e32 v86, v10
	v_cvt_f32_f16_sdwa v89, v11 dst_sel:DWORD dst_unused:UNUSED_PAD src0_sel:WORD_1
	v_cvt_f32_f16_e32 v88, v11
	v_cvt_f32_f16_sdwa v91, v12 dst_sel:DWORD dst_unused:UNUSED_PAD src0_sel:WORD_1
	v_cvt_f32_f16_e32 v90, v12
	v_cvt_f32_f16_sdwa v93, v13 dst_sel:DWORD dst_unused:UNUSED_PAD src0_sel:WORD_1
	v_cvt_f32_f16_e32 v92, v13
	s_waitcnt lgkmcnt(0)
	v_lshl_or_b32 v2, v62, 8, v71
	v_lshl_or_b32 v6, v63, 8, v71
	v_lshl_or_b32 v10, v64, 8, v71
	buffer_load_dwordx4 v[2:5], v2, s[20:23], 0 offen
	buffer_load_dwordx4 v[6:9], v6, s[20:23], 0 offen
	buffer_load_dwordx4 v[10:13], v10, s[20:23], 0 offen
	v_mfma_f32_4x4x1_16b_f32 v[22:25], v66, v78, v[22:25]
	v_mfma_f32_4x4x1_16b_f32 v[26:29], v66, v79, v[26:29]
	v_mfma_f32_4x4x1_16b_f32 v[30:33], v66, v80, v[30:33]
	v_mfma_f32_4x4x1_16b_f32 v[34:37], v66, v81, v[34:37]
	v_mfma_f32_4x4x1_16b_f32 v[38:41], v66, v82, v[38:41]
	v_mfma_f32_4x4x1_16b_f32 v[42:45], v66, v83, v[42:45]
	v_mfma_f32_4x4x1_16b_f32 v[46:49], v66, v84, v[46:49]
	v_mfma_f32_4x4x1_16b_f32 v[50:53], v66, v85, v[50:53]
	v_mfma_f32_4x4x1_16b_f32 v[22:25], v67, v86, v[22:25]
	v_mfma_f32_4x4x1_16b_f32 v[26:29], v67, v87, v[26:29]
	v_mfma_f32_4x4x1_16b_f32 v[30:33], v67, v88, v[30:33]
	v_mfma_f32_4x4x1_16b_f32 v[34:37], v67, v89, v[34:37]
	v_mfma_f32_4x4x1_16b_f32 v[38:41], v67, v90, v[38:41]
	v_mfma_f32_4x4x1_16b_f32 v[42:45], v67, v91, v[42:45]
	v_mfma_f32_4x4x1_16b_f32 v[46:49], v67, v92, v[46:49]
	v_mfma_f32_4x4x1_16b_f32 v[50:53], v67, v93, v[50:53]
	v_add_u32_e32 v72, 48, v72
	s_add_i32 s2, s2, 3
.Ll1g_loopO:
	s_add_i32 s5, s2, 6
	s_cmp_ge_i32 s5, s3
	s_cbranch_scc1 .Ll1g_tailO
	ds_read_b32 v65, v72
	ds_read_b32 v66, v72 offset:16
	ds_read_b32 v67, v72 offset:32
	s_lshl_b32 s4, s5, 2
	v_add_u32_e32 v73, s4, v70
	ds_read2_b32 v[62:63], v73 offset0:192 offset1:193
	ds_read_b32 v64, v73 offset:776
	s_waitcnt vmcnt(3)
	v_cvt_f32_f16_sdwa v55, v14 dst_sel:DWORD dst_unused:UNUSED_PAD src0_sel:WORD_1
	v_cvt_f32_f16_e32 v54, v14
	v_cvt_f32_f16_sdwa v57, v15 dst_sel:DWORD dst_unused:UNUSED_PAD src0_sel:WORD_1
	v_cvt_f32_f16_e32 v56, v15
	v_cvt_f32_f16_sdwa v59, v16 dst_sel:DWORD dst_unused:UNUSED_PAD src0_sel:WORD_1
	v_cvt_f32_f16_e32 v58, v16
	v_cvt_f32_f16_sdwa v61, v17 dst_sel:DWORD dst_unused:UNUSED_PAD src0_sel:WORD_1
	v_cvt_f32_f16_e32 v60, v17
	v_cvt_f32_f16_sdwa v79, v18 dst_sel:DWORD dst_unused:UNUSED_PAD src0_sel:WORD_1
	v_cvt_f32_f16_e32 v78, v18
	v_cvt_f32_f16_sdwa v81, v19 dst_sel:DWORD dst_unused:UNUSED_PAD src0_sel:WORD_1
	v_cvt_f32_f16_e32 v80, v19
	v_cvt_f32_f16_sdwa v83, v20 dst_sel:DWORD dst_unused:UNUSED_PAD src0_sel:WORD_1
	v_cvt_f32_f16_e32 v82, v20
	v_cvt_f32_f16_sdwa v85, v21 dst_sel:DWORD dst_unused:UNUSED_PAD src0_sel:WORD_1
	v_cvt_f32_f16_e32 v84, v21
	s_waitcnt lgkmcnt(2)
	v_mfma_f32_4x4x1_16b_f32 v[22:25], v65, v54, v[22:25]
	v_mfma_f32_4x4x1_16b_f32 v[26:29], v65, v55, v[26:29]
	v_mfma_f32_4x4x1_16b_f32 v[30:33], v65, v56, v[30:33]
	v_mfma_f32_4x4x1_16b_f32 v[34:37], v65, v57, v[34:37]
	v_mfma_f32_4x4x1_16b_f32 v[38:41], v65, v58, v[38:41]
	v_mfma_f32_4x4x1_16b_f32 v[42:45], v65, v59, v[42:45]
	v_mfma_f32_4x4x1_16b_f32 v[46:49], v65, v60, v[46:49]
	v_mfma_f32_4x4x1_16b_f32 v[50:53], v65, v61, v[50:53]
	v_cvt_f32_f16_sdwa v87, v74 dst_sel:DWORD dst_unused:UNUSED_PAD src0_sel:WORD_1
	v_cvt_f32_f16_e32 v86, v74
	v_cvt_f32_f16_sdwa v89, v75 dst_sel:DWORD dst_unused:UNUSED_PAD src0_sel:WORD_1
	v_cvt_f32_f16_e32 v88, v75
	v_cvt_f32_f16_sdwa v91, v76 dst_sel:DWORD dst_unused:UNUSED_PAD src0_sel:WORD_1
	v_cvt_f32_f16_e32 v90, v76
	v_cvt_f32_f16_sdwa v93, v77 dst_sel:DWORD dst_unused:UNUSED_PAD src0_sel:WORD_1
	v_cvt_f32_f16_e32 v92, v77
	s_waitcnt lgkmcnt(0)
	v_lshl_or_b32 v14, v62, 8, v71
	v_lshl_or_b32 v18, v63, 8, v71
	v_lshl_or_b32 v74, v64, 8, v71
	buffer_load_dwordx4 v[14:17], v14, s[20:23], 0 offen
	buffer_load_dwordx4 v[18:21], v18, s[20:23], 0 offen
	buffer_load_dwordx4 v[74:77], v74, s[20:23], 0 offen
	v_mfma_f32_4x4x1_16b_f32 v[22:25], v66, v78, v[22:25]
	v_mfma_f32_4x4x1_16b_f32 v[26:29], v66, v79, v[26:29]
	v_mfma_f32_4x4x1_16b_f32 v[30:33], v66, v80, v[30:33]
	v_mfma_f32_4x4x1_16b_f32 v[34:37], v66, v81, v[34:37]
	v_mfma_f32_4x4x1_16b_f32 v[38:41], v66, v82, v[38:41]
	v_mfma_f32_4x4x1_16b_f32 v[42:45], v66, v83, v[42:45]
	v_mfma_f32_4x4x1_16b_f32 v[46:49], v66, v84, v[46:49]
	v_mfma_f32_4x4x1_16b_f32 v[50:53], v66, v85, v[50:53]
	v_mfma_f32_4x4x1_16b_f32 v[22:25], v67, v86, v[22:25]
	v_mfma_f32_4x4x1_16b_f32 v[26:29], v67, v87, v[26:29]
	v_mfma_f32_4x4x1_16b_f32 v[30:33], v67, v88, v[30:33]
	v_mfma_f32_4x4x1_16b_f32 v[34:37], v67, v89, v[34:37]
	v_mfma_f32_4x4x1_16b_f32 v[38:41], v67, v90, v[38:41]
	v_mfma_f32_4x4x1_16b_f32 v[42:45], v67, v91, v[42:45]
	v_mfma_f32_4x4x1_16b_f32 v[46:49], v67, v92, v[46:49]
	v_mfma_f32_4x4x1_16b_f32 v[50:53], v67, v93, v[50:53]
	v_add_u32_e32 v72, 48, v72
	s_add_i32 s2, s2, 3
	s_branch .Ll1g_loopE
.Ll1g_tailE:
	s_add_i32 s5, s2, 3
	s_cmp_ge_i32 s5, s3
	s_cbranch_scc1 .Ll1g_lastE
	ds_read_b32 v65, v72
	ds_read_b32 v66, v72 offset:16
	ds_read_b32 v67, v72 offset:32
	s_waitcnt vmcnt(3)
	v_cvt_f32_f16_sdwa v55, v2 dst_sel:DWORD dst_unused:UNUSED_PAD src0_sel:WORD_1
	v_cvt_f32_f16_e32 v54, v2
	v_cvt_f32_f16_sdwa v57, v3 dst_sel:DWORD dst_unused:UNUSED_PAD src0_sel:WORD_1
	v_cvt_f32_f16_e32 v56, v3
	v_cvt_f32_f16_sdwa v59, v4 dst_sel:DWORD dst_unused:UNUSED_PAD src0_sel:WORD_1
	v_cvt_f32_f16_e32 v58, v4
	v_cvt_f32_f16_sdwa v61, v5 dst_sel:DWORD dst_unused:UNUSED_PAD src0_sel:WORD_1
	v_cvt_f32_f16_e32 v60, v5
	v_cvt_f32_f16_sdwa v79, v6 dst_sel:DWORD dst_unused:UNUSED_PAD src0_sel:WORD_1
	v_cvt_f32_f16_e32 v78, v6
	v_cvt_f32_f16_sdwa v81, v7 dst_sel:DWORD dst_unused:UNUSED_PAD src0_sel:WORD_1
	v_cvt_f32_f16_e32 v80, v7
	v_cvt_f32_f16_sdwa v83, v8 dst_sel:DWORD dst_unused:UNUSED_PAD src0_sel:WORD_1
	v_cvt_f32_f16_e32 v82, v8
	v_cvt_f32_f16_sdwa v85, v9 dst_sel:DWORD dst_unused:UNUSED_PAD src0_sel:WORD_1
	v_cvt_f32_f16_e32 v84, v9
	s_waitcnt lgkmcnt(0)
	v_mfma_f32_4x4x1_16b_f32 v[22:25], v65, v54, v[22:25]
	v_mfma_f32_4x4x1_16b_f32 v[26:29], v65, v55, v[26:29]
	v_mfma_f32_4x4x1_16b_f32 v[30:33], v65, v56, v[30:33]
	v_mfma_f32_4x4x1_16b_f32 v[34:37], v65, v57, v[34:37]
	v_mfma_f32_4x4x1_16b_f32 v[38:41], v65, v58, v[38:41]
	v_mfma_f32_4x4x1_16b_f32 v[42:45], v65, v59, v[42:45]
	v_mfma_f32_4x4x1_16b_f32 v[46:49], v65, v60, v[46:49]
	v_mfma_f32_4x4x1_16b_f32 v[50:53], v65, v61, v[50:53]
	v_cvt_f32_f16_sdwa v87, v10 dst_sel:DWORD dst_unused:UNUSED_PAD src0_sel:WORD_1
	v_cvt_f32_f16_e32 v86, v10
	v_cvt_f32_f16_sdwa v89, v11 dst_sel:DWORD dst_unused:UNUSED_PAD src0_sel:WORD_1
	v_cvt_f32_f16_e32 v88, v11
	v_cvt_f32_f16_sdwa v91, v12 dst_sel:DWORD dst_unused:UNUSED_PAD src0_sel:WORD_1
	v_cvt_f32_f16_e32 v90, v12
	v_cvt_f32_f16_sdwa v93, v13 dst_sel:DWORD dst_unused:UNUSED_PAD src0_sel:WORD_1
	v_cvt_f32_f16_e32 v92, v13
	v_mfma_f32_4x4x1_16b_f32 v[22:25], v66, v78, v[22:25]
	v_mfma_f32_4x4x1_16b_f32 v[26:29], v66, v79, v[26:29]
	v_mfma_f32_4x4x1_16b_f32 v[30:33], v66, v80, v[30:33]
	v_mfma_f32_4x4x1_16b_f32 v[34:37], v66, v81, v[34:37]
	v_mfma_f32_4x4x1_16b_f32 v[38:41], v66, v82, v[38:41]
	v_mfma_f32_4x4x1_16b_f32 v[42:45], v66, v83, v[42:45]
	v_mfma_f32_4x4x1_16b_f32 v[46:49], v66, v84, v[46:49]
	v_mfma_f32_4x4x1_16b_f32 v[50:53], v66, v85, v[50:53]
	v_mfma_f32_4x4x1_16b_f32 v[22:25], v67, v86, v[22:25]
	v_mfma_f32_4x4x1_16b_f32 v[26:29], v67, v87, v[26:29]
	v_mfma_f32_4x4x1_16b_f32 v[30:33], v67, v88, v[30:33]
	v_mfma_f32_4x4x1_16b_f32 v[34:37], v67, v89, v[34:37]
	v_mfma_f32_4x4x1_16b_f32 v[38:41], v67, v90, v[38:41]
	v_mfma_f32_4x4x1_16b_f32 v[42:45], v67, v91, v[42:45]
	v_mfma_f32_4x4x1_16b_f32 v[46:49], v67, v92, v[46:49]
	v_mfma_f32_4x4x1_16b_f32 v[50:53], v67, v93, v[50:53]
	v_add_u32_e32 v72, 48, v72
	s_add_i32 s2, s2, 3
	ds_read_b32 v65, v72
	ds_read_b32 v66, v72 offset:16
	ds_read_b32 v67, v72 offset:32
	s_waitcnt vmcnt(0)
	v_cvt_f32_f16_sdwa v55, v14 dst_sel:DWORD dst_unused:UNUSED_PAD src0_sel:WORD_1
	v_cvt_f32_f16_e32 v54, v14
	v_cvt_f32_f16_sdwa v57, v15 dst_sel:DWORD dst_unused:UNUSED_PAD src0_sel:WORD_1
	v_cvt_f32_f16_e32 v56, v15
	v_cvt_f32_f16_sdwa v59, v16 dst_sel:DWORD dst_unused:UNUSED_PAD src0_sel:WORD_1
	v_cvt_f32_f16_e32 v58, v16
	v_cvt_f32_f16_sdwa v61, v17 dst_sel:DWORD dst_unused:UNUSED_PAD src0_sel:WORD_1
	v_cvt_f32_f16_e32 v60, v17
	v_cvt_f32_f16_sdwa v79, v18 dst_sel:DWORD dst_unused:UNUSED_PAD src0_sel:WORD_1
	v_cvt_f32_f16_e32 v78, v18
	v_cvt_f32_f16_sdwa v81, v19 dst_sel:DWORD dst_unused:UNUSED_PAD src0_sel:WORD_1
	v_cvt_f32_f16_e32 v80, v19
	v_cvt_f32_f16_sdwa v83, v20 dst_sel:DWORD dst_unused:UNUSED_PAD src0_sel:WORD_1
	v_cvt_f32_f16_e32 v82, v20
	v_cvt_f32_f16_sdwa v85, v21 dst_sel:DWORD dst_unused:UNUSED_PAD src0_sel:WORD_1
	v_cvt_f32_f16_e32 v84, v21
	s_waitcnt lgkmcnt(0)
	v_mfma_f32_4x4x1_16b_f32 v[22:25], v65, v54, v[22:25]
	v_mfma_f32_4x4x1_16b_f32 v[26:29], v65, v55, v[26:29]
	v_mfma_f32_4x4x1_16b_f32 v[30:33], v65, v56, v[30:33]
	v_mfma_f32_4x4x1_16b_f32 v[34:37], v65, v57, v[34:37]
	v_mfma_f32_4x4x1_16b_f32 v[38:41], v65, v58, v[38:41]
	v_mfma_f32_4x4x1_16b_f32 v[42:45], v65, v59, v[42:45]
	v_mfma_f32_4x4x1_16b_f32 v[46:49], v65, v60, v[46:49]
	v_mfma_f32_4x4x1_16b_f32 v[50:53], v65, v61, v[50:53]
	v_cvt_f32_f16_sdwa v87, v74 dst_sel:DWORD dst_unused:UNUSED_PAD src0_sel:WORD_1
	v_cvt_f32_f16_e32 v86, v74
	v_cvt_f32_f16_sdwa v89, v75 dst_sel:DWORD dst_unused:UNUSED_PAD src0_sel:WORD_1
	v_cvt_f32_f16_e32 v88, v75
	v_cvt_f32_f16_sdwa v91, v76 dst_sel:DWORD dst_unused:UNUSED_PAD src0_sel:WORD_1
	v_cvt_f32_f16_e32 v90, v76
	v_cvt_f32_f16_sdwa v93, v77 dst_sel:DWORD dst_unused:UNUSED_PAD src0_sel:WORD_1
	v_cvt_f32_f16_e32 v92, v77
	v_mfma_f32_4x4x1_16b_f32 v[22:25], v66, v78, v[22:25]
	v_mfma_f32_4x4x1_16b_f32 v[26:29], v66, v79, v[26:29]
	v_mfma_f32_4x4x1_16b_f32 v[30:33], v66, v80, v[30:33]
	v_mfma_f32_4x4x1_16b_f32 v[34:37], v66, v81, v[34:37]
	v_mfma_f32_4x4x1_16b_f32 v[38:41], v66, v82, v[38:41]
	v_mfma_f32_4x4x1_16b_f32 v[42:45], v66, v83, v[42:45]
	v_mfma_f32_4x4x1_16b_f32 v[46:49], v66, v84, v[46:49]
	v_mfma_f32_4x4x1_16b_f32 v[50:53], v66, v85, v[50:53]
	v_mfma_f32_4x4x1_16b_f32 v[22:25], v67, v86, v[22:25]
	v_mfma_f32_4x4x1_16b_f32 v[26:29], v67, v87, v[26:29]
	v_mfma_f32_4x4x1_16b_f32 v[30:33], v67, v88, v[30:33]
	v_mfma_f32_4x4x1_16b_f32 v[34:37], v67, v89, v[34:37]
	v_mfma_f32_4x4x1_16b_f32 v[38:41], v67, v90, v[38:41]
	v_mfma_f32_4x4x1_16b_f32 v[42:45], v67, v91, v[42:45]
	v_mfma_f32_4x4x1_16b_f32 v[46:49], v67, v92, v[46:49]
	v_mfma_f32_4x4x1_16b_f32 v[50:53], v67, v93, v[50:53]
	s_branch .Ll1g_done
.Ll1g_lastE:
	ds_read_b32 v65, v72
	ds_read_b32 v66, v72 offset:16
	ds_read_b32 v67, v72 offset:32
	s_waitcnt vmcnt(0)
	v_cvt_f32_f16_sdwa v55, v2 dst_sel:DWORD dst_unused:UNUSED_PAD src0_sel:WORD_1
	v_cvt_f32_f16_e32 v54, v2
	v_cvt_f32_f16_sdwa v57, v3 dst_sel:DWORD dst_unused:UNUSED_PAD src0_sel:WORD_1
	v_cvt_f32_f16_e32 v56, v3
	v_cvt_f32_f16_sdwa v59, v4 dst_sel:DWORD dst_unused:UNUSED_PAD src0_sel:WORD_1
	v_cvt_f32_f16_e32 v58, v4
	v_cvt_f32_f16_sdwa v61, v5 dst_sel:DWORD dst_unused:UNUSED_PAD src0_sel:WORD_1
	v_cvt_f32_f16_e32 v60, v5
	v_cvt_f32_f16_sdwa v79, v6 dst_sel:DWORD dst_unused:UNUSED_PAD src0_sel:WORD_1
	v_cvt_f32_f16_e32 v78, v6
	v_cvt_f32_f16_sdwa v81, v7 dst_sel:DWORD dst_unused:UNUSED_PAD src0_sel:WORD_1
	v_cvt_f32_f16_e32 v80, v7
	v_cvt_f32_f16_sdwa v83, v8 dst_sel:DWORD dst_unused:UNUSED_PAD src0_sel:WORD_1
	v_cvt_f32_f16_e32 v82, v8
	v_cvt_f32_f16_sdwa v85, v9 dst_sel:DWORD dst_unused:UNUSED_PAD src0_sel:WORD_1
	v_cvt_f32_f16_e32 v84, v9
	s_waitcnt lgkmcnt(0)
	v_mfma_f32_4x4x1_16b_f32 v[22:25], v65, v54, v[22:25]
	v_mfma_f32_4x4x1_16b_f32 v[26:29], v65, v55, v[26:29]
	v_mfma_f32_4x4x1_16b_f32 v[30:33], v65, v56, v[30:33]
	v_mfma_f32_4x4x1_16b_f32 v[34:37], v65, v57, v[34:37]
	v_mfma_f32_4x4x1_16b_f32 v[38:41], v65, v58, v[38:41]
	v_mfma_f32_4x4x1_16b_f32 v[42:45], v65, v59, v[42:45]
	v_mfma_f32_4x4x1_16b_f32 v[46:49], v65, v60, v[46:49]
	v_mfma_f32_4x4x1_16b_f32 v[50:53], v65, v61, v[50:53]
	v_cvt_f32_f16_sdwa v87, v10 dst_sel:DWORD dst_unused:UNUSED_PAD src0_sel:WORD_1
	v_cvt_f32_f16_e32 v86, v10
	v_cvt_f32_f16_sdwa v89, v11 dst_sel:DWORD dst_unused:UNUSED_PAD src0_sel:WORD_1
	v_cvt_f32_f16_e32 v88, v11
	v_cvt_f32_f16_sdwa v91, v12 dst_sel:DWORD dst_unused:UNUSED_PAD src0_sel:WORD_1
	v_cvt_f32_f16_e32 v90, v12
	v_cvt_f32_f16_sdwa v93, v13 dst_sel:DWORD dst_unused:UNUSED_PAD src0_sel:WORD_1
	v_cvt_f32_f16_e32 v92, v13
	v_mfma_f32_4x4x1_16b_f32 v[22:25], v66, v78, v[22:25]
	v_mfma_f32_4x4x1_16b_f32 v[26:29], v66, v79, v[26:29]
	v_mfma_f32_4x4x1_16b_f32 v[30:33], v66, v80, v[30:33]
	v_mfma_f32_4x4x1_16b_f32 v[34:37], v66, v81, v[34:37]
	v_mfma_f32_4x4x1_16b_f32 v[38:41], v66, v82, v[38:41]
	v_mfma_f32_4x4x1_16b_f32 v[42:45], v66, v83, v[42:45]
	v_mfma_f32_4x4x1_16b_f32 v[46:49], v66, v84, v[46:49]
	v_mfma_f32_4x4x1_16b_f32 v[50:53], v66, v85, v[50:53]
	v_mfma_f32_4x4x1_16b_f32 v[22:25], v67, v86, v[22:25]
	v_mfma_f32_4x4x1_16b_f32 v[26:29], v67, v87, v[26:29]
	v_mfma_f32_4x4x1_16b_f32 v[30:33], v67, v88, v[30:33]
	v_mfma_f32_4x4x1_16b_f32 v[34:37], v67, v89, v[34:37]
	v_mfma_f32_4x4x1_16b_f32 v[38:41], v67, v90, v[38:41]
	v_mfma_f32_4x4x1_16b_f32 v[42:45], v67, v91, v[42:45]
	v_mfma_f32_4x4x1_16b_f32 v[46:49], v67, v92, v[46:49]
	v_mfma_f32_4x4x1_16b_f32 v[50:53], v67, v93, v[50:53]
	s_branch .Ll1g_done
.Ll1g_tailO:
	s_add_i32 s5, s2, 3
	s_cmp_ge_i32 s5, s3
	s_cbranch_scc1 .Ll1g_lastO
	ds_read_b32 v65, v72
	ds_read_b32 v66, v72 offset:16
	ds_read_b32 v67, v72 offset:32
	s_waitcnt vmcnt(3)
	v_cvt_f32_f16_sdwa v55, v14 dst_sel:DWORD dst_unused:UNUSED_PAD src0_sel:WORD_1
	v_cvt_f32_f16_e32 v54, v14
	v_cvt_f32_f16_sdwa v57, v15 dst_sel:DWORD dst_unused:UNUSED_PAD src0_sel:WORD_1
	v_cvt_f32_f16_e32 v56, v15
	v_cvt_f32_f16_sdwa v59, v16 dst_sel:DWORD dst_unused:UNUSED_PAD src0_sel:WORD_1
	v_cvt_f32_f16_e32 v58, v16
	v_cvt_f32_f16_sdwa v61, v17 dst_sel:DWORD dst_unused:UNUSED_PAD src0_sel:WORD_1
	v_cvt_f32_f16_e32 v60, v17
	v_cvt_f32_f16_sdwa v79, v18 dst_sel:DWORD dst_unused:UNUSED_PAD src0_sel:WORD_1
	v_cvt_f32_f16_e32 v78, v18
	v_cvt_f32_f16_sdwa v81, v19 dst_sel:DWORD dst_unused:UNUSED_PAD src0_sel:WORD_1
	v_cvt_f32_f16_e32 v80, v19
	v_cvt_f32_f16_sdwa v83, v20 dst_sel:DWORD dst_unused:UNUSED_PAD src0_sel:WORD_1
	v_cvt_f32_f16_e32 v82, v20
	v_cvt_f32_f16_sdwa v85, v21 dst_sel:DWORD dst_unused:UNUSED_PAD src0_sel:WORD_1
	v_cvt_f32_f16_e32 v84, v21
	s_waitcnt lgkmcnt(0)
	v_mfma_f32_4x4x1_16b_f32 v[22:25], v65, v54, v[22:25]
	v_mfma_f32_4x4x1_16b_f32 v[26:29], v65, v55, v[26:29]
	v_mfma_f32_4x4x1_16b_f32 v[30:33], v65, v56, v[30:33]
	v_mfma_f32_4x4x1_16b_f32 v[34:37], v65, v57, v[34:37]
	v_mfma_f32_4x4x1_16b_f32 v[38:41], v65, v58, v[38:41]
	v_mfma_f32_4x4x1_16b_f32 v[42:45], v65, v59, v[42:45]
	v_mfma_f32_4x4x1_16b_f32 v[46:49], v65, v60, v[46:49]
	v_mfma_f32_4x4x1_16b_f32 v[50:53], v65, v61, v[50:53]
	v_cvt_f32_f16_sdwa v87, v74 dst_sel:DWORD dst_unused:UNUSED_PAD src0_sel:WORD_1
	v_cvt_f32_f16_e32 v86, v74
	v_cvt_f32_f16_sdwa v89, v75 dst_sel:DWORD dst_unused:UNUSED_PAD src0_sel:WORD_1
	v_cvt_f32_f16_e32 v88, v75
	v_cvt_f32_f16_sdwa v91, v76 dst_sel:DWORD dst_unused:UNUSED_PAD src0_sel:WORD_1
	v_cvt_f32_f16_e32 v90, v76
	v_cvt_f32_f16_sdwa v93, v77 dst_sel:DWORD dst_unused:UNUSED_PAD src0_sel:WORD_1
	v_cvt_f32_f16_e32 v92, v77
	v_mfma_f32_4x4x1_16b_f32 v[22:25], v66, v78, v[22:25]
	v_mfma_f32_4x4x1_16b_f32 v[26:29], v66, v79, v[26:29]
	v_mfma_f32_4x4x1_16b_f32 v[30:33], v66, v80, v[30:33]
	v_mfma_f32_4x4x1_16b_f32 v[34:37], v66, v81, v[34:37]
	v_mfma_f32_4x4x1_16b_f32 v[38:41], v66, v82, v[38:41]
	v_mfma_f32_4x4x1_16b_f32 v[42:45], v66, v83, v[42:45]
	v_mfma_f32_4x4x1_16b_f32 v[46:49], v66, v84, v[46:49]
	v_mfma_f32_4x4x1_16b_f32 v[50:53], v66, v85, v[50:53]
	v_mfma_f32_4x4x1_16b_f32 v[22:25], v67, v86, v[22:25]
	v_mfma_f32_4x4x1_16b_f32 v[26:29], v67, v87, v[26:29]
	v_mfma_f32_4x4x1_16b_f32 v[30:33], v67, v88, v[30:33]
	v_mfma_f32_4x4x1_16b_f32 v[34:37], v67, v89, v[34:37]
	v_mfma_f32_4x4x1_16b_f32 v[38:41], v67, v90, v[38:41]
	v_mfma_f32_4x4x1_16b_f32 v[42:45], v67, v91, v[42:45]
	v_mfma_f32_4x4x1_16b_f32 v[46:49], v67, v92, v[46:49]
	v_mfma_f32_4x4x1_16b_f32 v[50:53], v67, v93, v[50:53]
	v_add_u32_e32 v72, 48, v72
	s_add_i32 s2, s2, 3
	ds_read_b32 v65, v72
	ds_read_b32 v66, v72 offset:16
	ds_read_b32 v67, v72 offset:32
	s_waitcnt vmcnt(0)
	v_cvt_f32_f16_sdwa v55, v2 dst_sel:DWORD dst_unused:UNUSED_PAD src0_sel:WORD_1
	v_cvt_f32_f16_e32 v54, v2
	v_cvt_f32_f16_sdwa v57, v3 dst_sel:DWORD dst_unused:UNUSED_PAD src0_sel:WORD_1
	v_cvt_f32_f16_e32 v56, v3
	v_cvt_f32_f16_sdwa v59, v4 dst_sel:DWORD dst_unused:UNUSED_PAD src0_sel:WORD_1
	v_cvt_f32_f16_e32 v58, v4
	v_cvt_f32_f16_sdwa v61, v5 dst_sel:DWORD dst_unused:UNUSED_PAD src0_sel:WORD_1
	v_cvt_f32_f16_e32 v60, v5
	v_cvt_f32_f16_sdwa v79, v6 dst_sel:DWORD dst_unused:UNUSED_PAD src0_sel:WORD_1
	v_cvt_f32_f16_e32 v78, v6
	v_cvt_f32_f16_sdwa v81, v7 dst_sel:DWORD dst_unused:UNUSED_PAD src0_sel:WORD_1
	v_cvt_f32_f16_e32 v80, v7
	v_cvt_f32_f16_sdwa v83, v8 dst_sel:DWORD dst_unused:UNUSED_PAD src0_sel:WORD_1
	v_cvt_f32_f16_e32 v82, v8
	v_cvt_f32_f16_sdwa v85, v9 dst_sel:DWORD dst_unused:UNUSED_PAD src0_sel:WORD_1
	v_cvt_f32_f16_e32 v84, v9
	s_waitcnt lgkmcnt(0)
	v_mfma_f32_4x4x1_16b_f32 v[22:25], v65, v54, v[22:25]
	v_mfma_f32_4x4x1_16b_f32 v[26:29], v65, v55, v[26:29]
	v_mfma_f32_4x4x1_16b_f32 v[30:33], v65, v56, v[30:33]
	v_mfma_f32_4x4x1_16b_f32 v[34:37], v65, v57, v[34:37]
	v_mfma_f32_4x4x1_16b_f32 v[38:41], v65, v58, v[38:41]
	v_mfma_f32_4x4x1_16b_f32 v[42:45], v65, v59, v[42:45]
	v_mfma_f32_4x4x1_16b_f32 v[46:49], v65, v60, v[46:49]
	v_mfma_f32_4x4x1_16b_f32 v[50:53], v65, v61, v[50:53]
	v_cvt_f32_f16_sdwa v87, v10 dst_sel:DWORD dst_unused:UNUSED_PAD src0_sel:WORD_1
	v_cvt_f32_f16_e32 v86, v10
	v_cvt_f32_f16_sdwa v89, v11 dst_sel:DWORD dst_unused:UNUSED_PAD src0_sel:WORD_1
	v_cvt_f32_f16_e32 v88, v11
	v_cvt_f32_f16_sdwa v91, v12 dst_sel:DWORD dst_unused:UNUSED_PAD src0_sel:WORD_1
	v_cvt_f32_f16_e32 v90, v12
	v_cvt_f32_f16_sdwa v93, v13 dst_sel:DWORD dst_unused:UNUSED_PAD src0_sel:WORD_1
	v_cvt_f32_f16_e32 v92, v13
	v_mfma_f32_4x4x1_16b_f32 v[22:25], v66, v78, v[22:25]
	v_mfma_f32_4x4x1_16b_f32 v[26:29], v66, v79, v[26:29]
	v_mfma_f32_4x4x1_16b_f32 v[30:33], v66, v80, v[30:33]
	v_mfma_f32_4x4x1_16b_f32 v[34:37], v66, v81, v[34:37]
	v_mfma_f32_4x4x1_16b_f32 v[38:41], v66, v82, v[38:41]
	v_mfma_f32_4x4x1_16b_f32 v[42:45], v66, v83, v[42:45]
	v_mfma_f32_4x4x1_16b_f32 v[46:49], v66, v84, v[46:49]
	v_mfma_f32_4x4x1_16b_f32 v[50:53], v66, v85, v[50:53]
	v_mfma_f32_4x4x1_16b_f32 v[22:25], v67, v86, v[22:25]
	v_mfma_f32_4x4x1_16b_f32 v[26:29], v67, v87, v[26:29]
	v_mfma_f32_4x4x1_16b_f32 v[30:33], v67, v88, v[30:33]
	v_mfma_f32_4x4x1_16b_f32 v[34:37], v67, v89, v[34:37]
	v_mfma_f32_4x4x1_16b_f32 v[38:41], v67, v90, v[38:41]
	v_mfma_f32_4x4x1_16b_f32 v[42:45], v67, v91, v[42:45]
	v_mfma_f32_4x4x1_16b_f32 v[46:49], v67, v92, v[46:49]
	v_mfma_f32_4x4x1_16b_f32 v[50:53], v67, v93, v[50:53]
	s_branch .Ll1g_done
.Ll1g_lastO:
	ds_read_b32 v65, v72
	ds_read_b32 v66, v72 offset:16
	ds_read_b32 v67, v72 offset:32
	s_waitcnt vmcnt(0)
	v_cvt_f32_f16_sdwa v55, v14 dst_sel:DWORD dst_unused:UNUSED_PAD src0_sel:WORD_1
	v_cvt_f32_f16_e32 v54, v14
	v_cvt_f32_f16_sdwa v57, v15 dst_sel:DWORD dst_unused:UNUSED_PAD src0_sel:WORD_1
	v_cvt_f32_f16_e32 v56, v15
	v_cvt_f32_f16_sdwa v59, v16 dst_sel:DWORD dst_unused:UNUSED_PAD src0_sel:WORD_1
	v_cvt_f32_f16_e32 v58, v16
	v_cvt_f32_f16_sdwa v61, v17 dst_sel:DWORD dst_unused:UNUSED_PAD src0_sel:WORD_1
	v_cvt_f32_f16_e32 v60, v17
	v_cvt_f32_f16_sdwa v79, v18 dst_sel:DWORD dst_unused:UNUSED_PAD src0_sel:WORD_1
	v_cvt_f32_f16_e32 v78, v18
	v_cvt_f32_f16_sdwa v81, v19 dst_sel:DWORD dst_unused:UNUSED_PAD src0_sel:WORD_1
	v_cvt_f32_f16_e32 v80, v19
	v_cvt_f32_f16_sdwa v83, v20 dst_sel:DWORD dst_unused:UNUSED_PAD src0_sel:WORD_1
	v_cvt_f32_f16_e32 v82, v20
	v_cvt_f32_f16_sdwa v85, v21 dst_sel:DWORD dst_unused:UNUSED_PAD src0_sel:WORD_1
	v_cvt_f32_f16_e32 v84, v21
	s_waitcnt lgkmcnt(0)
	v_mfma_f32_4x4x1_16b_f32 v[22:25], v65, v54, v[22:25]
	v_mfma_f32_4x4x1_16b_f32 v[26:29], v65, v55, v[26:29]
	v_mfma_f32_4x4x1_16b_f32 v[30:33], v65, v56, v[30:33]
	v_mfma_f32_4x4x1_16b_f32 v[34:37], v65, v57, v[34:37]
	v_mfma_f32_4x4x1_16b_f32 v[38:41], v65, v58, v[38:41]
	v_mfma_f32_4x4x1_16b_f32 v[42:45], v65, v59, v[42:45]
	v_mfma_f32_4x4x1_16b_f32 v[46:49], v65, v60, v[46:49]
	v_mfma_f32_4x4x1_16b_f32 v[50:53], v65, v61, v[50:53]
	v_cvt_f32_f16_sdwa v87, v74 dst_sel:DWORD dst_unused:UNUSED_PAD src0_sel:WORD_1
	v_cvt_f32_f16_e32 v86, v74
	v_cvt_f32_f16_sdwa v89, v75 dst_sel:DWORD dst_unused:UNUSED_PAD src0_sel:WORD_1
	v_cvt_f32_f16_e32 v88, v75
	v_cvt_f32_f16_sdwa v91, v76 dst_sel:DWORD dst_unused:UNUSED_PAD src0_sel:WORD_1
	v_cvt_f32_f16_e32 v90, v76
	v_cvt_f32_f16_sdwa v93, v77 dst_sel:DWORD dst_unused:UNUSED_PAD src0_sel:WORD_1
	v_cvt_f32_f16_e32 v92, v77
	v_mfma_f32_4x4x1_16b_f32 v[22:25], v66, v78, v[22:25]
	v_mfma_f32_4x4x1_16b_f32 v[26:29], v66, v79, v[26:29]
	v_mfma_f32_4x4x1_16b_f32 v[30:33], v66, v80, v[30:33]
	v_mfma_f32_4x4x1_16b_f32 v[34:37], v66, v81, v[34:37]
	v_mfma_f32_4x4x1_16b_f32 v[38:41], v66, v82, v[38:41]
	v_mfma_f32_4x4x1_16b_f32 v[42:45], v66, v83, v[42:45]
	v_mfma_f32_4x4x1_16b_f32 v[46:49], v66, v84, v[46:49]
	v_mfma_f32_4x4x1_16b_f32 v[50:53], v66, v85, v[50:53]
	v_mfma_f32_4x4x1_16b_f32 v[22:25], v67, v86, v[22:25]
	v_mfma_f32_4x4x1_16b_f32 v[26:29], v67, v87, v[26:29]
	v_mfma_f32_4x4x1_16b_f32 v[30:33], v67, v88, v[30:33]
	v_mfma_f32_4x4x1_16b_f32 v[34:37], v67, v89, v[34:37]
	v_mfma_f32_4x4x1_16b_f32 v[38:41], v67, v90, v[38:41]
	v_mfma_f32_4x4x1_16b_f32 v[42:45], v67, v91, v[42:45]
	v_mfma_f32_4x4x1_16b_f32 v[46:49], v67, v92, v[46:49]
	v_mfma_f32_4x4x1_16b_f32 v[50:53], v67, v93, v[50:53]
.Ll1g_done:
	s_setprio 0
	v_add_u32_e32 v6, v70, v71
	s_nop 4
	v_cvt_pk_f16_f32 v2, v22, v26
	v_cvt_pk_f16_f32 v3, v30, v34
	v_cvt_pk_f16_f32 v4, v38, v42
	v_cvt_pk_f16_f32 v5, v46, v50
	ds_write_b128 v6, v[2:5]
	v_cvt_pk_f16_f32 v2, v23, v27
	v_cvt_pk_f16_f32 v3, v31, v35
	v_cvt_pk_f16_f32 v4, v39, v43
	v_cvt_pk_f16_f32 v5, v47, v51
	ds_write_b128 v6, v[2:5] offset:256
	v_cvt_pk_f16_f32 v2, v24, v28
	v_cvt_pk_f16_f32 v3, v32, v36
	v_cvt_pk_f16_f32 v4, v40, v44
	v_cvt_pk_f16_f32 v5, v48, v52
	ds_write_b128 v6, v[2:5] offset:512
	v_cvt_pk_f16_f32 v2, v25, v29
	v_cvt_pk_f16_f32 v3, v33, v37
	v_cvt_pk_f16_f32 v4, v41, v45
	v_cvt_pk_f16_f32 v5, v49, v53
	ds_write_b128 v6, v[2:5] offset:768

.LBB2_57:
	s_endpgm
	s_nop 0
	s_nop 0
	s_nop 0
	s_nop 0
	s_nop 0
	s_nop 0
	s_nop 0
	s_nop 0
	s_nop 0
	s_nop 0
	s_nop 0
	s_nop 0
	s_nop 0
	s_nop 0
	s_nop 0
	s_nop 0
	s_nop 0
	s_nop 0
	s_nop 0
	s_nop 0
	s_nop 0
	s_nop 0
	s_nop 0
	s_nop 0
	s_nop 0
	s_nop 0
	s_nop 0
	s_nop 0
	s_nop 0
	s_nop 0
	s_nop 0
	s_nop 0
	s_nop 0
	s_nop 0
	s_nop 0
	s_nop 0
	s_nop 0
	s_nop 0
	s_nop 0
	s_nop 0
	s_nop 0
	s_nop 0
	s_nop 0
	s_nop 0
	s_endpgm
